# speedup vs baseline: 1.0238x; 1.0062x over previous
_Z6gemm4pILi96ELi2ELi0EEvPKtS1_iii7EpiArgs:
	s_load_dwordx4 s[4:7], s[0:1], 0x10
	s_load_dwordx2 s[8:9], s[0:1], 0x8
	s_waitcnt lgkmcnt(0)
	s_mov_b32 s62, s2
	s_add_u32 s84, s8, 0xe3a0100
	s_addc_u32 s85, s9, 0
	s_mul_i32 s63, s62, 0x6200
	s_add_u32 s68, s8, 0x2d60000
	s_addc_u32 s69, s9, 0
	s_add_u32 s68, s68, s63
	s_addc_u32 s69, s69, 0
	s_mul_i32 s63, s62, 0x4200
	s_add_u32 s70, s8, 0x18c0000
	s_addc_u32 s71, s9, 0
	s_add_u32 s70, s70, s63
	s_addc_u32 s71, s71, 0
	v_lshlrev_b32_e32 v216, 4, v0
	v_mov_b32_e32 v217, v0
	s_mov_b32 s79, 0xaaab
	s_mov_b32 s80, 0x10000
	s_ashr_i32 s3, s4, 31
	s_lshr_b32 s3, s3, 24
	s_mul_hi_i32 s5, s5, 0x2aaaaaab
	s_add_i32 s3, s4, s3
	s_ashr_i32 s10, s3, 8
	s_lshr_b32 s3, s5, 31
	s_ashr_i32 s7, s5, 5
	s_add_i32 s7, s7, s3
	s_mul_i32 s4, s7, s10
	s_ashr_i32 s3, s4, 31
	s_lshr_b32 s3, s3, 29
	s_add_i32 s5, s4, s3
	s_ashr_i32 s3, s5, 3
	s_and_b32 s5, s5, -8
	s_sub_i32 s4, s4, s5
	s_ashr_i32 s5, s2, 31
	s_lshr_b32 s5, s5, 29
	s_add_i32 s14, s2, s5
	s_and_b32 s5, s14, -8
	s_sub_i32 s12, s2, s5
	s_add_i32 s13, s3, 1
	s_cmp_ge_i32 s12, s4
	s_cbranch_scc0 .LBB2_2
	s_mul_i32 s2, s13, s4
	s_sub_i32 s4, s12, s4
	s_mul_i32 s4, s4, s3
	s_add_i32 s11, s2, s4
	s_load_dwordx2 s[2:3], s[0:1], 0x0
	s_ashr_i32 s4, s14, 3
	s_cbranch_execz .LBB2_3
	s_branch .LBB2_4

.LBB2_6:
	s_mul_i32 s18, s18, s16
	s_sub_i32 s5, s17, s18
	s_add_i32 s5, s5, s7
	s_lshl_b32 s7, s5, 8
	s_ashr_i32 s8, s7, 31
	s_mul_i32 s8, s10, s8
	s_mul_hi_u32 s9, s10, s7
	v_mul_lo_u32 v7, v1, s4
	v_add_u32_e32 v1, 64, v1
	s_add_i32 s8, s9, s8
	s_mul_i32 s9, s11, s7
	s_lshl_b32 s5, s4, 2
	v_lshrrev_b32_e32 v1, 1, v1
	s_add_i32 s8, s8, s9
	s_mul_i32 s9, s10, s7
	v_xor_b32_e32 v1, v1, v0
	s_waitcnt lgkmcnt(0)
	s_add_u32 s16, s2, s9
	v_add_u32_e32 v4, s5, v4
	v_lshlrev_b32_e32 v1, 3, v1
	s_addc_u32 s2, s3, s8
	s_load_dwordx4 s[64:67], s[84:85], 0x0
	s_mov_b32 m0, s28
	v_add_lshl_u32 v180, v3, v7, 1
	v_add_lshl_u32 v179, v4, v3, 1
	v_lshl_add_u32 v3, s4, 6, v7
	v_and_b32_e32 v1, 56, v1
	s_and_b32 s17, s2, 0xffff
	s_mov_b32 s18, s14
	s_mov_b32 s19, s15
	s_add_i32 s33, s28, 0x2000
	v_add_lshl_u32 v181, v1, v3, 1
	buffer_load_dwordx4 v180, s[16:19], 0 offen lds
	s_mov_b32 m0, s33
	s_add_i32 s34, s28, 0x4000
	s_lshl_b32 s29, s4, 8
	buffer_load_dwordx4 v181, s[16:19], 0 offen lds
	s_mov_b32 m0, s34
	s_add_i32 s35, s28, 0x6000
	buffer_load_dwordx4 v180, s[16:19], s29 offen lds
	s_mov_b32 m0, s35
	s_add_i32 s36, s28, 0x13000
	buffer_load_dwordx4 v181, s[16:19], s29 offen lds
	s_mov_b32 m0, s36
	s_and_b32 s2, s30, 0xffffff00
	buffer_load_dwordx4 v179, s[12:15], 0 offen lds
	v_add_u32_e32 v1, s5, v6
	s_cmpk_eq_i32 s2, 0x100
	s_cselect_b64 s[22:23], -1, 0
	s_cmpk_lg_i32 s2, 0x100
	v_add_lshl_u32 v182, v1, v5, 1
	s_cbranch_scc1 .LBB2_8
	s_lshl_b32 s2, s27, 10
	s_add_i32 s2, s2, 0
	s_add_i32 m0, s2, 0x13000
	s_nop 0
	buffer_load_dwordx4 v182, s[12:15], 0 offen lds
	s_barrier

.LBB2_10:
	s_and_b32 s25, s38, 1
	s_add_i32 s38, s28, 0x8000
	s_mov_b32 s18, s14
	s_mov_b32 s19, s15
	s_mov_b32 m0, s38
	s_add_i32 s39, s28, 0xa000
	buffer_load_dwordx4 v180, s[16:19], s2 offen lds
	s_mov_b32 m0, s39
	v_and_b32_e32 v1, 15, v0
	buffer_load_dwordx4 v181, s[16:19], s2 offen lds
	v_lshrrev_b32_e32 v178, 4, v2
	v_lshrrev_b32_e32 v2, 1, v0
	s_mul_i32 s3, s25, 48
	s_lshr_b32 s24, s30, 7
	v_lshlrev_b32_e32 v4, 7, v1
	v_or_b32_e32 v5, s3, v1
	v_bitop3_b32 v2, v178, v2, 7 bitop3:0x78
	s_load_dwordx2 s[0:1], s[0:1], 0x20
	v_bfe_u32 v3, v0, 1, 3
	v_lshl_or_b32 v4, s24, 12, v4
	v_lshlrev_b32_e32 v5, 7, v5
	v_lshlrev_b32_e32 v2, 4, v2
	s_ashr_i32 s3, s6, 31
	v_or_b32_e32 v6, v2, v4
	v_or_b32_e32 v184, v2, v5
	v_bitop3_b32 v2, v178, v3, 4 bitop3:0x36
	s_lshr_b32 s3, s3, 26
	v_lshlrev_b32_e32 v2, 4, v2
	s_add_i32 s3, s6, s3
	v_or_b32_e32 v3, v2, v4
	v_or_b32_e32 v185, v2, v5
	s_ashr_i32 s30, s3, 6
	v_mov_b32_e32 v5, 0
	s_cmpk_lt_i32 s6, 0xc0
	v_add_u32_e32 v187, 0, v6
	v_add_u32_e32 v186, 0, v3
	v_mov_b32_e32 v4, v5
	v_mov_b32_e32 v3, v5
	v_mov_b32_e32 v2, v5
	v_mov_b32_e32 v13, v5
	v_mov_b32_e32 v12, v5
	v_mov_b32_e32 v11, v5
	v_mov_b32_e32 v10, v5
	v_mov_b32_e32 v21, v5
	v_mov_b32_e32 v20, v5
	v_mov_b32_e32 v19, v5
	v_mov_b32_e32 v18, v5
	v_mov_b32_e32 v29, v5
	v_mov_b32_e32 v28, v5
	v_mov_b32_e32 v27, v5
	v_mov_b32_e32 v26, v5
	v_mov_b32_e32 v37, v5
	v_mov_b32_e32 v36, v5
	v_mov_b32_e32 v35, v5
	v_mov_b32_e32 v34, v5
	v_mov_b32_e32 v45, v5
	v_mov_b32_e32 v44, v5
	v_mov_b32_e32 v43, v5
	v_mov_b32_e32 v42, v5
	v_mov_b32_e32 v97, v5
	v_mov_b32_e32 v96, v5
	v_mov_b32_e32 v95, v5
	v_mov_b32_e32 v94, v5
	v_mov_b32_e32 v89, v5
	v_mov_b32_e32 v88, v5
	v_mov_b32_e32 v87, v5
	v_mov_b32_e32 v86, v5
	v_mov_b32_e32 v81, v5
	v_mov_b32_e32 v80, v5
	v_mov_b32_e32 v79, v5
	v_mov_b32_e32 v78, v5
	v_mov_b32_e32 v73, v5
	v_mov_b32_e32 v72, v5
	v_mov_b32_e32 v71, v5
	v_mov_b32_e32 v70, v5
	v_mov_b32_e32 v65, v5
	v_mov_b32_e32 v64, v5
	v_mov_b32_e32 v63, v5
	v_mov_b32_e32 v62, v5
	v_mov_b32_e32 v57, v5
	v_mov_b32_e32 v56, v5
	v_mov_b32_e32 v55, v5
	v_mov_b32_e32 v54, v5
	v_mov_b32_e32 v49, v5
	v_mov_b32_e32 v48, v5
	v_mov_b32_e32 v47, v5
	v_mov_b32_e32 v46, v5
	v_mov_b32_e32 v41, v5
	v_mov_b32_e32 v40, v5
	v_mov_b32_e32 v39, v5
	v_mov_b32_e32 v38, v5
	v_mov_b32_e32 v33, v5
	v_mov_b32_e32 v32, v5
	v_mov_b32_e32 v31, v5
	v_mov_b32_e32 v30, v5
	v_mov_b32_e32 v25, v5
	v_mov_b32_e32 v24, v5
	v_mov_b32_e32 v23, v5
	v_mov_b32_e32 v22, v5
	v_mov_b32_e32 v17, v5
	v_mov_b32_e32 v16, v5
	v_mov_b32_e32 v15, v5
	v_mov_b32_e32 v14, v5
	v_mov_b32_e32 v9, v5
	v_mov_b32_e32 v8, v5
	v_mov_b32_e32 v7, v5
	v_mov_b32_e32 v6, v5
	v_mov_b32_e32 v93, v5
	v_mov_b32_e32 v92, v5
	v_mov_b32_e32 v91, v5
	v_mov_b32_e32 v90, v5
	v_mov_b32_e32 v85, v5
	v_mov_b32_e32 v84, v5
	v_mov_b32_e32 v83, v5
	v_mov_b32_e32 v82, v5
	v_mov_b32_e32 v77, v5
	v_mov_b32_e32 v76, v5
	v_mov_b32_e32 v75, v5
	v_mov_b32_e32 v74, v5
	v_mov_b32_e32 v69, v5
	v_mov_b32_e32 v68, v5
	v_mov_b32_e32 v67, v5
	v_mov_b32_e32 v66, v5
	v_mov_b32_e32 v61, v5
	v_mov_b32_e32 v60, v5
	v_mov_b32_e32 v59, v5
	v_mov_b32_e32 v58, v5
	v_mov_b32_e32 v53, v5
	v_mov_b32_e32 v52, v5
	v_mov_b32_e32 v51, v5
	v_mov_b32_e32 v50, v5
	s_barrier
	s_cbranch_scc1 .LBB2_21
	s_add_i32 s43, 0, 0x19000
	s_lshl_b32 s2, s27, 10
	s_add_i32 s45, s43, s2
	s_add_i32 s48, s2, 0
	s_add_i32 s2, 0, 0x10000
	v_add_u32_e32 v156, s2, v184
	v_add_u32_e32 v157, s2, v185
	s_add_i32 s2, 0, 0x10800
	v_mov_b32_e32 v50, 0
	v_add_u32_e32 v158, s2, v184
	v_add_u32_e32 v159, s2, v185
	s_add_i32 s2, 0, 0x11000
	v_cndmask_b32_e64 v2, 0, 1, s[22:23]
	s_add_i32 s40, s30, -2
	s_add_i32 s41, s28, 0xc000
	s_mov_b32 s42, 0
	s_add_i32 s44, s43, s44
	s_add_i32 s46, s48, 0x10000
	s_add_i32 s47, s48, 0x13000
	s_add_i32 s48, s48, 0x16000
	s_add_i32 s49, s28, 0xe000
	s_lshl_b32 s6, s6, 8
	s_movk_i32 s50, 0x4100
	v_add_u32_e32 v160, s2, v184
	v_add_u32_e32 v161, s2, v185
	v_cmp_ne_u32_e64 s[2:3], 1, v2
	s_add_i32 s51, 0, 0x13000
	s_add_i32 s52, 0, 0x13800
	s_add_i32 s53, 0, 0x14000
	s_add_i32 s54, 0, 0x16000
	s_add_i32 s55, 0, 0x16800
	s_add_i32 s56, 0, 0x17000
	s_add_i32 s57, 0, 0x19800
	s_add_i32 s58, 0, 0x1a000
	v_mov_b32_e32 v51, v50
	v_mov_b32_e32 v52, v50
	v_mov_b32_e32 v53, v50
	v_mov_b32_e32 v58, v50
	v_mov_b32_e32 v59, v50
	v_mov_b32_e32 v60, v50
	v_mov_b32_e32 v61, v50
	v_mov_b32_e32 v66, v50
	v_mov_b32_e32 v67, v50
	v_mov_b32_e32 v68, v50
	v_mov_b32_e32 v69, v50
	v_mov_b32_e32 v74, v50
	v_mov_b32_e32 v75, v50
	v_mov_b32_e32 v76, v50
	v_mov_b32_e32 v77, v50
	v_mov_b32_e32 v82, v50
	v_mov_b32_e32 v83, v50
	v_mov_b32_e32 v84, v50
	v_mov_b32_e32 v85, v50
	v_mov_b32_e32 v90, v50
	v_mov_b32_e32 v91, v50
	v_mov_b32_e32 v92, v50
	v_mov_b32_e32 v93, v50
	v_mov_b32_e32 v6, v50
	v_mov_b32_e32 v7, v50
	v_mov_b32_e32 v8, v50
	v_mov_b32_e32 v9, v50
	v_mov_b32_e32 v14, v50
	v_mov_b32_e32 v15, v50
	v_mov_b32_e32 v16, v50
	v_mov_b32_e32 v17, v50
	v_mov_b32_e32 v22, v50
	v_mov_b32_e32 v23, v50
	v_mov_b32_e32 v24, v50
	v_mov_b32_e32 v25, v50
	v_mov_b32_e32 v30, v50
	v_mov_b32_e32 v31, v50
	v_mov_b32_e32 v32, v50
	v_mov_b32_e32 v33, v50
	v_mov_b32_e32 v38, v50
	v_mov_b32_e32 v39, v50
	v_mov_b32_e32 v40, v50
	v_mov_b32_e32 v41, v50
	v_mov_b32_e32 v46, v50
	v_mov_b32_e32 v47, v50
	v_mov_b32_e32 v48, v50
	v_mov_b32_e32 v49, v50
	v_mov_b32_e32 v54, v50
	v_mov_b32_e32 v55, v50
	v_mov_b32_e32 v56, v50
	v_mov_b32_e32 v57, v50
	v_mov_b32_e32 v62, v50
	v_mov_b32_e32 v63, v50
	v_mov_b32_e32 v64, v50
	v_mov_b32_e32 v65, v50
	v_mov_b32_e32 v70, v50
	v_mov_b32_e32 v71, v50
	v_mov_b32_e32 v72, v50
	v_mov_b32_e32 v73, v50
	v_mov_b32_e32 v78, v50
	v_mov_b32_e32 v79, v50
	v_mov_b32_e32 v80, v50
	v_mov_b32_e32 v81, v50
	v_mov_b32_e32 v86, v50
	v_mov_b32_e32 v87, v50
	v_mov_b32_e32 v88, v50
	v_mov_b32_e32 v89, v50
	v_mov_b32_e32 v94, v50
	v_mov_b32_e32 v95, v50
	v_mov_b32_e32 v96, v50
	v_mov_b32_e32 v97, v50
	v_mov_b32_e32 v42, v50
	v_mov_b32_e32 v43, v50
	v_mov_b32_e32 v44, v50
	v_mov_b32_e32 v45, v50
	v_mov_b32_e32 v34, v50
	v_mov_b32_e32 v35, v50
	v_mov_b32_e32 v36, v50
	v_mov_b32_e32 v37, v50
	v_mov_b32_e32 v26, v50
	v_mov_b32_e32 v27, v50
	v_mov_b32_e32 v28, v50
	v_mov_b32_e32 v29, v50
	v_mov_b32_e32 v18, v50
	v_mov_b32_e32 v19, v50
	v_mov_b32_e32 v20, v50
	v_mov_b32_e32 v21, v50
	v_mov_b32_e32 v10, v50
	v_mov_b32_e32 v11, v50
	v_mov_b32_e32 v12, v50
	v_mov_b32_e32 v13, v50
	v_mov_b32_e32 v2, v50
	v_mov_b32_e32 v3, v50
	v_mov_b32_e32 v4, v50
	v_mov_b32_e32 v5, v50
	s_waitcnt lgkmcnt(0)
	s_mul_i32 s63, s62, 0xc000
	s_add_u32 s66, s66, s63
	s_addc_u32 s67, s67, 0
	s_lshl_b32 s63, s62, 15
	s_add_u32 s64, s64, s63
	s_addc_u32 s65, s65, 0
	s_sub_u32 s64, s64, 0xc000
	s_subb_u32 s65, s65, 0
	s_branch .LBB2_13
.LBB2_12:
	s_mov_b32 m0, s38
	s_nop 0
	buffer_load_dwordx4 v180, s[16:19], s59 offen lds
	s_mov_b32 m0, s39
	s_nop 0
	buffer_load_dwordx4 v181, s[16:19], s59 offen lds
	s_waitcnt vmcnt(5)
	s_waitcnt lgkmcnt(0)
	s_barrier
	s_setprio 1
	s_waitcnt lgkmcnt(5)
	v_mfma_f32_16x16x32_bf16 v[42:45], v[134:137], v[106:109], v[42:45]
	s_cmp_lt_u32 s72, 6
	s_waitcnt lgkmcnt(3)
	v_mfma_f32_16x16x32_bf16 v[34:37], v[142:145], v[106:109], v[34:37]
	s_cselect_b32 s76, s68, s70
	s_waitcnt lgkmcnt(1)
	v_mfma_f32_16x16x32_bf16 v[26:29], v[150:153], v[106:109], v[26:29]
	s_cselect_b32 s77, s69, s71
	v_mfma_f32_16x16x32_bf16 v[106:109], v[150:153], v[122:125], v[30:33]
	s_cselect_b32 s78, s79, s80
	v_mfma_f32_16x16x32_bf16 v[162:165], v[134:137], v[122:125], v[46:49]
	s_cselect_b32 s81, 0, 6
	s_waitcnt lgkmcnt(0)
	v_mfma_f32_16x16x32_bf16 v[30:33], v[146:149], v[110:113], v[26:29]
	s_cselect_b64 s[82:83], -1, 0
	v_mfma_f32_16x16x32_bf16 v[26:29], v[146:149], v[126:129], v[106:109]
	s_sub_u32 s81, s72, s81
	v_mfma_f32_16x16x32_bf16 v[18:21], v[134:137], v[98:101], v[18:21]
	s_lshl_b32 s81, s81, 9
	v_mfma_f32_16x16x32_bf16 v[106:109], v[134:137], v[114:117], v[22:25]
	v_add_u32_e32 v222, s81, v217
	v_mfma_f32_16x16x32_bf16 v[46:49], v[130:133], v[110:113], v[42:45]
	v_mul_u32_u24_e32 v223, s78, v222
	v_mfma_f32_16x16x32_bf16 v[42:45], v[130:133], v[126:129], v[162:165]
	v_lshrrev_b32_e32 v223, 25, v223
	v_mfma_f32_16x16x32_bf16 v[162:165], v[142:145], v[122:125], v[38:41]
	v_lshlrev_b32_e32 v222, 3, v222
	v_mfma_f32_16x16x32_bf16 v[22:25], v[130:133], v[102:105], v[18:21]
	v_lshl_add_u32 v222, v223, 7, v222
	v_mfma_f32_16x16x32_bf16 v[18:21], v[130:133], v[118:121], v[106:109]
	v_cvt_pk_f16_f32 v224, v218, v219
	v_mfma_f32_16x16x32_bf16 v[10:13], v[142:145], v[98:101], v[10:13]
	v_cvt_pk_f16_f32 v225, v220, v221
	v_mfma_f32_16x16x32_bf16 v[106:109], v[142:145], v[114:117], v[14:17]
	v_cvt_pk_bf16_f32 v226, v218, v219
	v_mfma_f32_16x16x32_bf16 v[2:5], v[150:153], v[98:101], v[2:5]
	v_cvt_pk_bf16_f32 v227, v220, v221
	v_mfma_f32_16x16x32_bf16 v[98:101], v[150:153], v[114:117], v[6:9]
	v_cndmask_b32_e64 v224, v226, v224, s[82:83]
	v_mfma_f32_16x16x32_bf16 v[38:41], v[138:141], v[110:113], v[34:37]
	v_cndmask_b32_e64 v225, v227, v225, s[82:83]
	v_mfma_f32_16x16x32_bf16 v[34:37], v[138:141], v[126:129], v[162:165]
	global_store_dwordx2 v222, v[224:225], s[76:77] sc0 sc1
	v_mfma_f32_16x16x32_bf16 v[14:17], v[138:141], v[102:105], v[10:13]
	v_mfma_f32_16x16x32_bf16 v[10:13], v[138:141], v[118:121], v[106:109]
	v_mfma_f32_16x16x32_bf16 v[6:9], v[146:149], v[102:105], v[2:5]
	v_mfma_f32_16x16x32_bf16 v[2:5], v[146:149], v[118:121], v[98:101]
	s_setprio 0
	s_barrier
	s_add_i32 s42, s42, 2
	s_addk_i32 s50, 0x100
	s_cmp_ge_i32 s42, s40
	s_cbranch_scc1 .LBB2_21

.LBB2_15:
	s_add_i32 s60, s50, 0xffffc000
	ds_read_b128 v[122:125], v187 offset:16384
	ds_read_b128 v[114:117], v187 offset:18432
	ds_read_b128 v[126:129], v186 offset:16384
	ds_read_b128 v[118:121], v186 offset:18432
	s_waitcnt vmcnt(7)
	s_waitcnt lgkmcnt(4)
	s_barrier
	s_setprio 1
	v_mfma_f32_16x16x32_bf16 v[94:97], v[150:153], v[106:109], v[94:97]
	s_lshr_b32 s72, s42, 1
	v_mfma_f32_16x16x32_bf16 v[86:89], v[142:145], v[106:109], v[86:89]
	s_min_u32 s72, s72, 9
	v_mfma_f32_16x16x32_bf16 v[78:81], v[134:137], v[106:109], v[78:81]
	s_lshl_b32 s73, s72, 13
	v_mfma_f32_16x16x32_bf16 v[70:73], v[150:153], v[98:101], v[70:73]
	s_cmp_lt_u32 s72, 6
	v_mfma_f32_16x16x32_bf16 v[62:65], v[142:145], v[98:101], v[62:65]
	s_cselect_b32 s74, s66, s64
	v_mfma_f32_16x16x32_bf16 v[54:57], v[134:137], v[98:101], v[54:57]
	s_cselect_b32 s75, s67, s65
	v_mfma_f32_16x16x32_bf16 v[94:97], v[146:149], v[110:113], v[94:97]
	s_add_u32 s74, s74, s73
	v_mfma_f32_16x16x32_bf16 v[86:89], v[138:141], v[110:113], v[86:89]
	s_addc_u32 s75, s75, 0
	v_mfma_f32_16x16x32_bf16 v[78:81], v[130:133], v[110:113], v[78:81]
	global_load_dwordx4 v[218:221], v216, s[74:75] sc0 sc1 nt
	v_mfma_f32_16x16x32_bf16 v[70:73], v[146:149], v[102:105], v[70:73]
	v_mfma_f32_16x16x32_bf16 v[62:65], v[138:141], v[102:105], v[62:65]
	v_mfma_f32_16x16x32_bf16 v[54:57], v[130:133], v[102:105], v[54:57]
	s_waitcnt lgkmcnt(2)
	v_mfma_f32_16x16x32_bf16 v[90:93], v[150:153], v[122:125], v[90:93]
	v_mfma_f32_16x16x32_bf16 v[82:85], v[142:145], v[122:125], v[82:85]
	v_mfma_f32_16x16x32_bf16 v[74:77], v[134:137], v[122:125], v[74:77]
	v_mfma_f32_16x16x32_bf16 v[66:69], v[150:153], v[114:117], v[66:69]
	v_mfma_f32_16x16x32_bf16 v[58:61], v[142:145], v[114:117], v[58:61]
	v_mfma_f32_16x16x32_bf16 v[50:53], v[134:137], v[114:117], v[50:53]
	s_waitcnt lgkmcnt(0)
	v_mfma_f32_16x16x32_bf16 v[90:93], v[146:149], v[126:129], v[90:93]
	v_mfma_f32_16x16x32_bf16 v[82:85], v[138:141], v[126:129], v[82:85]
	v_mfma_f32_16x16x32_bf16 v[74:77], v[130:133], v[126:129], v[74:77]
	v_mfma_f32_16x16x32_bf16 v[66:69], v[146:149], v[118:121], v[66:69]
	v_mfma_f32_16x16x32_bf16 v[58:61], v[138:141], v[118:121], v[58:61]
	v_mfma_f32_16x16x32_bf16 v[50:53], v[130:133], v[118:121], v[50:53]
	s_setprio 0
	s_barrier
	s_mov_b32 m0, s31
	v_add_u32_e32 v130, s51, v184
	v_add_u32_e32 v131, s51, v185
	v_add_u32_e32 v138, s52, v184
	v_add_u32_e32 v139, s52, v185
	v_add_u32_e32 v146, s53, v184
	v_add_u32_e32 v147, s53, v185
	ds_read_b128 v[134:137], v130
	ds_read_b128 v[130:133], v131
	ds_read_b128 v[142:145], v138
	ds_read_b128 v[138:141], v139
	ds_read_b128 v[150:153], v146
	ds_read_b128 v[146:149], v147
	buffer_load_dwordx4 v154, s[12:15], s60 offen lds
	s_and_b64 vcc, exec, s[4:5]
	s_cbranch_vccnz .LBB2_17
	s_mov_b32 m0, s46
	s_nop 0
	buffer_load_dwordx4 v155, s[12:15], s60 offen lds
